# FoX item loop: the queue ticket atomic is requested before the end-of-item drain + barrier so its round trip overlaps the store drain
# speedup vs baseline: 1.0138x; 1.0013x over previous
.LBB0_641:
	s_and_saveexec_b64 s[6:7], s[4:5]
	s_cbranch_execz .Lfq_noissue
	s_mov_b64 s[10:11], exec
	v_mbcnt_lo_u32_b32 v2, s10, 0
	v_mbcnt_hi_u32_b32 v2, s11, v2
	v_cmp_eq_u32_e32 vcc, 0, v2
	s_and_saveexec_b64 s[8:9], vcc
	s_cbranch_execz .Lfq_noat
	s_bcnt1_i32_b64 s10, s[10:11]
	v_mov_b32_e32 v4, s10
	global_atomic_add v4, v3, v4, s[14:15] sc0

.Lfq_noissue:
	s_or_b64 exec, exec, s[6:7]
	s_waitcnt vmcnt(0) lgkmcnt(0)
	s_barrier
	s_and_saveexec_b64 s[6:7], s[4:5]
	s_cbranch_execz .LBB0_645
.LBB0_644:
	s_waitcnt vmcnt(0)
	v_readfirstlane_b32 s8, v4
	v_mov_b32_e32 v4, s41
	s_nop 0
	v_add_u32_e32 v2, s8, v2
	ds_write_b32 v4, v2
